# speedup vs baseline: 1.0172x; 1.0172x over previous
_Z15k_scatter_gemm1PKiS0_PiPjPyPKfPK6__halfS5_S5_PS6_PfSA_:
	s_cmpk_gt_u32 s2, 0x186
	s_mov_b64 s[4:5], -1
	s_cbranch_scc0 .LBB1_22
	s_load_dwordx2 s[26:27], s[0:1], 0x28
	s_load_dwordx2 s[10:11], s[0:1], 0x30
	s_load_dwordx4 s[28:31], s[0:1], 0x38
	v_lshlrev_b32_e32 v92, 4, v0
	v_add_u32_e32 v93, 0x1000, v92
	v_add_u32_e32 v94, 0x2000, v92
	v_add_u32_e32 v95, 0x3000, v92
	v_add_u32_e32 v96, 0x4000, v92
	v_add_u32_e32 v97, 0x5000, v92
	v_add_u32_e32 v98, 0x6000, v92
	v_add_u32_e32 v99, 0x7000, v92
	v_add_u32_e32 v100, 0x8000, v92
	v_lshlrev_b32_e32 v101, 2, v0
	s_movk_i32 s3, 0x80
	v_cmp_gt_u32_e64 s[8:9], s3, v0
	s_waitcnt lgkmcnt(0)
	global_load_dwordx4 v[104:107], v92, s[10:11]
	global_load_dwordx4 v[108:111], v93, s[10:11]
	global_load_dwordx4 v[112:115], v94, s[10:11]
	global_load_dwordx4 v[116:119], v95, s[10:11]
	global_load_dwordx4 v[120:123], v96, s[10:11]
	global_load_dwordx4 v[124:127], v97, s[10:11]
	global_load_dwordx4 v[128:131], v98, s[10:11]
	global_load_dwordx4 v[132:135], v99, s[10:11]
	s_and_saveexec_b64 s[4:5], s[8:9]
	global_load_dwordx4 v[136:139], v100, s[10:11]
	global_load_dword v140, v101, s[28:29]
	global_load_dword v141, v101, s[30:31]
	s_mov_b64 exec, s[4:5]
	s_lshl_b32 s3, s2, 2
	v_lshrrev_b32_e32 v14, 6, v0
	s_add_i32 s4, s3, 0xfffff9e4
	v_or_b32_e32 v2, s4, v14
	s_movk_i32 s4, 2250
	v_cmp_gt_i32_e32 vcc, s4, v2
	v_and_b32_e32 v1, 15, v0
	v_and_b32_e32 v66, 48, v0
	v_mov_b32_e32 v67, 0
	s_and_saveexec_b64 s[6:7], vcc
	s_cbranch_execz .Lg1_noval
	v_lshl_or_b32 v2, v2, 4, v1
	v_ashrrev_i32_e32 v3, 31, v2
	v_lshlrev_b64 v[2:3], 9, v[2:3]
	v_lshl_add_u64 v[2:3], s[26:27], 0, v[2:3]
	v_lshl_add_u64 v[16:17], v[2:3], 0, v[66:67]
	global_load_dwordx4 v[38:41], v[16:17], off offset:448
	global_load_dwordx4 v[34:37], v[16:17], off offset:384
	global_load_dwordx4 v[46:49], v[16:17], off offset:320
	global_load_dwordx4 v[42:45], v[16:17], off offset:256
	global_load_dwordx4 v[6:9], v[16:17], off offset:192
	global_load_dwordx4 v[18:21], v[16:17], off offset:128
	global_load_dwordx4 v[2:5], v[16:17], off offset:64
	global_load_dwordx4 v[10:13], v[16:17], off
	s_mov_b64 exec, s[6:7]
	s_waitcnt vmcnt(8)
	s_branch .Lg1_stage

.Lg1_stage:
	ds_write_b128 v92, v[104:107]
	ds_write_b128 v92, v[108:111] offset:4096
	ds_write_b128 v92, v[112:115] offset:8192
	ds_write_b128 v92, v[116:119] offset:12288
	ds_write_b128 v92, v[120:123] offset:16384
	ds_write_b128 v92, v[124:127] offset:20480
	ds_write_b128 v92, v[128:131] offset:24576
	ds_write_b128 v92, v[132:135] offset:28672
	s_and_saveexec_b64 s[4:5], s[8:9]
	ds_write_b128 v92, v[136:139] offset:32768
	ds_write2st64_b32 v101, v140, v141 offset0:204 offset1:206
	s_mov_b64 exec, s[4:5]
	s_waitcnt lgkmcnt(0)
	s_barrier
	s_and_saveexec_b64 s[6:7], vcc
	s_cbranch_execz .LBB1_21
	s_load_dwordx2 s[8:9], s[0:1], 0x58
	s_load_dwordx2 s[10:11], s[0:1], 0x48
	v_and_b32_e32 v15, 63, v0
	v_lshl_add_u64 v[68:69], s[26:27], 0, v[66:67]
	s_movk_i32 s4, 0x1100
	v_cmp_gt_u32_e32 vcc, 16, v15
	v_mul_u32_u24_e32 v15, 0x110, v1
	v_mul_u32_u24_e32 v17, 0x1100, v14
	v_mad_u32_u24 v22, v14, s4, v15
	v_lshlrev_b32_e32 v16, 4, v1
	v_add_u32_e32 v25, s3, v14
	v_lshlrev_b32_e32 v14, 4, v14
	v_bfe_u32 v80, v0, 4, 2
	v_or_b32_e32 v24, v17, v16
	v_mov_b32_e32 v17, v67
	v_lshl_or_b32 v82, s2, 6, v14
	v_mbcnt_lo_u32_b32 v14, -1, 0
	s_waitcnt lgkmcnt(0)
	v_lshl_add_u64 v[70:71], s[10:11], 0, v[16:17]
	v_or_b32_e32 v17, 4, v80
	v_mbcnt_hi_u32_b32 v84, -1, v14
	v_lshlrev_b32_e32 v23, 3, v80
	v_mul_u32_u24_e32 v16, 0x110, v80
	v_mul_u32_u24_e32 v17, 0x110, v17
	v_and_b32_e32 v14, 64, v84
	v_subrev_u32_e32 v67, 56, v25
	v_or_b32_e32 v81, 0xffff9e40, v1
	s_mov_b64 s[10:11], 0
	s_movk_i32 s3, 742
	v_add_u32_e32 v83, v66, v15
	v_xor_b32_e32 v85, 16, v84
	v_add_u32_e32 v86, 64, v14
	v_xor_b32_e32 v87, 32, v84
	v_add_u32_e32 v88, v22, v23
	v_add_u32_e32 v89, v24, v16
	v_add_u32_e32 v90, v24, v17
	s_movk_i32 s12, 741
	s_waitcnt vmcnt(0)
	s_branch .LBB1_19

_Z12k_fine_gemm1PKjPKyPKiPiS5_S5_S5_PKfPK6__halfS7_S7_PS8_PfSC_:
	s_cmpk_gt_u32 s2, 0x186
	s_mov_b64 s[4:5], -1
	s_cbranch_scc0 .LBB2_22
	s_load_dwordx2 s[26:27], s[0:1], 0x38
	s_load_dwordx2 s[10:11], s[0:1], 0x40
	s_load_dwordx4 s[28:31], s[0:1], 0x48
	v_lshlrev_b32_e32 v92, 4, v0
	v_add_u32_e32 v93, 0x1000, v92
	v_add_u32_e32 v94, 0x2000, v92
	v_add_u32_e32 v95, 0x3000, v92
	v_add_u32_e32 v96, 0x4000, v92
	v_add_u32_e32 v97, 0x5000, v92
	v_add_u32_e32 v98, 0x6000, v92
	v_add_u32_e32 v99, 0x7000, v92
	v_add_u32_e32 v100, 0x8000, v92
	v_lshlrev_b32_e32 v101, 2, v0
	s_movk_i32 s3, 0x80
	v_cmp_gt_u32_e64 s[8:9], s3, v0
	s_waitcnt lgkmcnt(0)
	global_load_dwordx4 v[104:107], v92, s[10:11]
	global_load_dwordx4 v[108:111], v93, s[10:11]
	global_load_dwordx4 v[112:115], v94, s[10:11]
	global_load_dwordx4 v[116:119], v95, s[10:11]
	global_load_dwordx4 v[120:123], v96, s[10:11]
	global_load_dwordx4 v[124:127], v97, s[10:11]
	global_load_dwordx4 v[128:131], v98, s[10:11]
	global_load_dwordx4 v[132:135], v99, s[10:11]
	s_and_saveexec_b64 s[4:5], s[8:9]
	global_load_dwordx4 v[136:139], v100, s[10:11]
	global_load_dword v140, v101, s[28:29]
	global_load_dword v141, v101, s[30:31]
	s_mov_b64 exec, s[4:5]
	s_lshl_b32 s3, s2, 2
	v_lshrrev_b32_e32 v14, 6, v0
	s_addk_i32 s3, 686
	v_add_u32_e32 v1, s3, v14
	s_movk_i32 s3, 0x186a
	v_cmp_gt_i32_e32 vcc, s3, v1
	v_and_b32_e32 v80, 15, v0
	v_and_b32_e32 v66, 48, v0
	v_mov_b32_e32 v67, 0
	s_and_saveexec_b64 s[6:7], vcc
	s_cbranch_execz .Lg2_noval
	v_lshl_or_b32 v2, v1, 4, v80
	v_ashrrev_i32_e32 v3, 31, v2
	v_lshlrev_b64 v[2:3], 9, v[2:3]
	v_lshl_add_u64 v[2:3], s[26:27], 0, v[2:3]
	v_lshl_add_u64 v[16:17], v[2:3], 0, v[66:67]
	global_load_dwordx4 v[38:41], v[16:17], off offset:448
	global_load_dwordx4 v[34:37], v[16:17], off offset:384
	global_load_dwordx4 v[26:29], v[16:17], off offset:320
	global_load_dwordx4 v[30:33], v[16:17], off offset:256
	global_load_dwordx4 v[6:9], v[16:17], off offset:192
	global_load_dwordx4 v[18:21], v[16:17], off offset:128
	global_load_dwordx4 v[2:5], v[16:17], off offset:64
	global_load_dwordx4 v[10:13], v[16:17], off
	s_mov_b64 exec, s[6:7]
	s_waitcnt vmcnt(8)
	s_branch .Lg2_stage

.Lg2_stage:
	ds_write_b128 v92, v[104:107]
	ds_write_b128 v92, v[108:111] offset:4096
	ds_write_b128 v92, v[112:115] offset:8192
	ds_write_b128 v92, v[116:119] offset:12288
	ds_write_b128 v92, v[120:123] offset:16384
	ds_write_b128 v92, v[124:127] offset:20480
	ds_write_b128 v92, v[128:131] offset:24576
	ds_write_b128 v92, v[132:135] offset:28672
	s_and_saveexec_b64 s[4:5], s[8:9]
	ds_write_b128 v92, v[136:139] offset:32768
	ds_write2st64_b32 v101, v140, v141 offset0:204 offset1:206
	s_mov_b64 exec, s[4:5]
	s_waitcnt lgkmcnt(0)
	s_barrier
	s_and_saveexec_b64 s[6:7], vcc
	s_cbranch_execz .LBB2_21
	s_load_dwordx2 s[8:9], s[0:1], 0x68
	s_load_dwordx2 s[10:11], s[0:1], 0x58
	v_and_b32_e32 v15, 63, v0
	s_movk_i32 s3, 0x1100
	v_cmp_gt_u32_e32 vcc, 16, v15
	v_mul_u32_u24_e32 v15, 0x110, v80
	v_mul_u32_u24_e32 v17, 0x1100, v14
	v_mad_u32_u24 v22, v14, s3, v15
	v_lshlrev_b32_e32 v16, 4, v80
	v_lshlrev_b32_e32 v14, 4, v14
	v_bfe_u32 v81, v0, 4, 2
	v_or_b32_e32 v24, v17, v16
	v_mov_b32_e32 v17, v67
	v_lshl_or_b32 v82, s2, 6, v14
	v_mbcnt_lo_u32_b32 v14, -1, 0
	s_waitcnt lgkmcnt(0)
	v_lshl_add_u64 v[70:71], s[10:11], 0, v[16:17]
	v_or_b32_e32 v17, 4, v81
	v_mbcnt_hi_u32_b32 v84, -1, v14
	v_lshlrev_b32_e32 v23, 3, v81
	v_mul_u32_u24_e32 v16, 0x110, v81
	v_mul_u32_u24_e32 v17, 0x110, v17
	v_and_b32_e32 v14, 64, v84
	v_lshl_add_u64 v[68:69], s[26:27], 0, v[66:67]
	v_or_b32_e32 v67, 0x2ae0, v80
	s_mov_b64 s[10:11], 0
	s_movk_i32 s3, 0x1285
	s_movk_i32 s14, 0x1286
	v_add_u32_e32 v83, v66, v15
	v_xor_b32_e32 v85, 16, v84
	v_add_u32_e32 v86, 64, v14
	v_xor_b32_e32 v87, 32, v84
	v_add_u32_e32 v88, v22, v23
	v_add_u32_e32 v89, v24, v16
	v_add_u32_e32 v90, v24, v17
	s_waitcnt vmcnt(0)
	s_branch .LBB2_19
.LBB2_18:
	s_or_b64 exec, exec, s[12:13]
	v_cvt_pk_f16_f32 v41, v40, v41
	v_cvt_pk_f16_f32 v40, v38, v39
	v_cvt_pk_f16_f32 v38, v62, v63
	v_add_u32_e32 v62, 0x8800, v88
	v_cvt_pk_f16_f32 v37, v36, v37
	v_cvt_pk_f16_f32 v36, v34, v35
	v_cvt_pk_f16_f32 v35, v56, v57
	v_cvt_pk_f16_f32 v34, v54, v55
	ds_write2_b64 v62, v[36:37], v[34:35] offset0:8 offset1:12
	v_cvt_pk_f16_f32 v35, v48, v49
	v_cvt_pk_f16_f32 v34, v46, v47
	v_cvt_pk_f16_f32 v37, v52, v53
	v_cvt_pk_f16_f32 v36, v50, v51
	v_cvt_pk_f16_f32 v39, v64, v65
	ds_write2_b64 v62, v[34:35], v[36:37] offset0:16 offset1:20
	v_cvt_pk_f16_f32 v35, v44, v45
	v_cvt_pk_f16_f32 v34, v42, v43
	v_cvt_pk_f16_f32 v37, v60, v61
	v_cvt_pk_f16_f32 v36, v58, v59
	ds_write2_b64 v62, v[40:41], v[38:39] offset1:4
	ds_write2_b64 v62, v[34:35], v[36:37] offset0:24 offset1:28
	ds_read_b128 v[34:37], v89 offset:34816
	v_add_u32_e32 v44, v81, v82
	v_add_u32_e32 v38, 0x2ae0, v44
	v_ashrrev_i32_e32 v39, 31, v38
	v_lshlrev_b64 v[38:39], 8, v[38:39]
	v_lshl_add_u64 v[42:43], v[70:71], 0, v[38:39]
	ds_read_b128 v[38:41], v90 offset:34816
	s_waitcnt lgkmcnt(1)
	global_store_dwordx4 v[42:43], v[34:37], off
	s_and_b64 s[4:5], exec, s[4:5]
	s_or_b64 s[10:11], s[4:5], s[10:11]
	v_add_u32_e32 v34, 0x2ae4, v44
	v_ashrrev_i32_e32 v35, 31, v34
	v_lshlrev_b64 v[34:35], 8, v[34:35]
	v_lshl_add_u64 v[34:35], v[70:71], 0, v[34:35]
	s_waitcnt lgkmcnt(0)
	global_store_dwordx4 v[34:35], v[38:41], off
	ds_read_b128 v[34:37], v90 offset:35904
	v_add_u32_e32 v82, 0x5e40, v82
	v_add_u32_e32 v38, 0x2ae8, v44
	v_ashrrev_i32_e32 v39, 31, v38
	v_lshlrev_b64 v[38:39], 8, v[38:39]
	v_lshl_add_u64 v[42:43], v[70:71], 0, v[38:39]
	ds_read_b128 v[38:41], v90 offset:36992
	s_waitcnt lgkmcnt(1)
	global_store_dwordx4 v[42:43], v[34:37], off
	s_nop 1
	v_add_u32_e32 v34, 0x2aec, v44
	v_ashrrev_i32_e32 v35, 31, v34
	v_lshlrev_b64 v[34:35], 8, v[34:35]
	v_lshl_add_u64 v[34:35], v[70:71], 0, v[34:35]
	s_waitcnt lgkmcnt(0)
	global_store_dwordx4 v[34:35], v[38:41], off
	s_waitcnt vmcnt(5)
	v_mov_b64_e32 v[36:37], v[32:33]
	v_mov_b64_e32 v[34:35], v[30:31]
	v_mov_b64_e32 v[32:33], v[24:25]
	v_mov_b64_e32 v[30:31], v[22:23]
	s_waitcnt vmcnt(4)
	v_mov_b64_e32 v[40:41], v[28:29]
	v_mov_b64_e32 v[38:39], v[26:27]
	v_mov_b64_e32 v[28:29], v[16:17]
	v_mov_b64_e32 v[26:27], v[14:15]
	s_andn2_b64 exec, exec, s[10:11]
	s_cbranch_execz .LBB2_21
